# round balancing: layers 1-3 limited to 7 resident blocks per CU through the static LDS size (rounds of 1792+1333 blocks instead of 2048+1077)
# speedup vs baseline: 1.0169x; 1.0169x over previous
	.amdhsa_kernel _Z12layer_kernelILb0ELi256ELi32EEvPKDv8_DF16_PKfPS0_PiS6_S6_S2_S4_S5_PfPK15HIP_vector_typeIiLj2EEPKi
		.amdhsa_group_segment_fixed_size 22000
		.amdhsa_private_segment_fixed_size 0
		.amdhsa_kernarg_size 352
		.amdhsa_user_sgpr_count 2
		.amdhsa_user_sgpr_dispatch_ptr 0
		.amdhsa_user_sgpr_queue_ptr 0
		.amdhsa_user_sgpr_kernarg_segment_ptr 1
		.amdhsa_user_sgpr_dispatch_id 0
		.amdhsa_user_sgpr_kernarg_preload_length 0
		.amdhsa_user_sgpr_kernarg_preload_offset 0
		.amdhsa_user_sgpr_private_segment_size 0
		.amdhsa_uses_dynamic_stack 0
		.amdhsa_enable_private_segment 0
		.amdhsa_system_sgpr_workgroup_id_x 1
		.amdhsa_system_sgpr_workgroup_id_y 0
		.amdhsa_system_sgpr_workgroup_id_z 0
		.amdhsa_system_sgpr_workgroup_info 0
		.amdhsa_system_vgpr_workitem_id 0
		.amdhsa_next_free_vgpr 64
		.amdhsa_next_free_sgpr 30
		.amdhsa_accum_offset 64
		.amdhsa_reserve_vcc 1
		.amdhsa_float_round_mode_32 0
		.amdhsa_float_round_mode_16_64 0
		.amdhsa_float_denorm_mode_32 3
		.amdhsa_float_denorm_mode_16_64 3
		.amdhsa_dx10_clamp 1
		.amdhsa_ieee_mode 1
		.amdhsa_fp16_overflow 0
		.amdhsa_tg_split 0
		.amdhsa_exception_fp_ieee_invalid_op 0
		.amdhsa_exception_fp_denorm_src 0
		.amdhsa_exception_fp_ieee_div_zero 0
		.amdhsa_exception_fp_ieee_overflow 0
		.amdhsa_exception_fp_ieee_underflow 0
		.amdhsa_exception_fp_ieee_inexact 0
		.amdhsa_exception_int_div_zero 0
	.end_amdhsa_kernel

amdhsa.kernels:
  - .agpr_count:     0
    .args:
      - .actual_access:  read_only
        .address_space:  global
        .offset:         0
        .size:           8
        .value_kind:     global_buffer
      - .address_space:  global
        .offset:         8
        .size:           8
        .value_kind:     global_buffer
      - .actual_access:  read_only
        .address_space:  global
        .offset:         16
        .size:           8
        .value_kind:     global_buffer
      - .actual_access:  read_only
        .address_space:  global
        .offset:         24
        .size:           8
        .value_kind:     global_buffer
      - .actual_access:  write_only
        .address_space:  global
        .offset:         32
        .size:           8
        .value_kind:     global_buffer
      - .actual_access:  read_only
        .address_space:  global
        .offset:         40
        .size:           8
        .value_kind:     global_buffer
      - .actual_access:  write_only
        .address_space:  global
        .offset:         48
        .size:           8
        .value_kind:     global_buffer
      - .actual_access:  write_only
        .address_space:  global
        .offset:         56
        .size:           8
        .value_kind:     global_buffer
    .group_segment_fixed_size: 6400
    .kernarg_segment_align: 8
    .kernarg_segment_size: 64
    .language:       OpenCL C
    .language_version:
      - 2
      - 0
    .max_flat_workgroup_size: 1024
    .name:           _Z17prep_count_kernelPKfPDv8_DF16_S0_S0_S2_PKiPiP15HIP_vector_typeIfLj4EE
    .private_segment_fixed_size: 0
    .sgpr_count:     22
    .sgpr_spill_count: 0
    .symbol:         _Z17prep_count_kernelPKfPDv8_DF16_S0_S0_S2_PKiPiP15HIP_vector_typeIfLj4EE.kd
    .uniform_work_group_size: 1
    .uses_dynamic_stack: false
    .vgpr_count:     22
    .vgpr_spill_count: 0
    .wavefront_size: 64
  - .agpr_count:     0
    .args:
      - .actual_access:  read_only
        .address_space:  global
        .offset:         0
        .size:           8
        .value_kind:     global_buffer
      - .actual_access:  read_only
        .address_space:  global
        .offset:         8
        .size:           8
        .value_kind:     global_buffer
      - .actual_access:  read_only
        .address_space:  global
        .offset:         16
        .size:           8
        .value_kind:     global_buffer
      - .actual_access:  write_only
        .address_space:  global
        .offset:         24
        .size:           8
        .value_kind:     global_buffer
      - .actual_access:  write_only
        .address_space:  global
        .offset:         32
        .size:           8
        .value_kind:     global_buffer
    .group_segment_fixed_size: 124704
    .kernarg_segment_align: 8
    .kernarg_segment_size: 40
    .language:       OpenCL C
    .language_version:
      - 2
      - 0
    .max_flat_workgroup_size: 1024
    .name:           _Z14scatter_kernelPKiS0_S0_PiP15HIP_vector_typeIiLj2EE
    .private_segment_fixed_size: 0
    .sgpr_count:     55
    .sgpr_spill_count: 0
    .symbol:         _Z14scatter_kernelPKiS0_S0_PiP15HIP_vector_typeIiLj2EE.kd
    .uniform_work_group_size: 1
    .uses_dynamic_stack: false
    .vgpr_count:     128
    .vgpr_spill_count: 0
    .wavefront_size: 64
  - .agpr_count:     0
    .args:
      - .actual_access:  read_only
        .address_space:  global
        .offset:         0
        .size:           8
        .value_kind:     global_buffer
      - .address_space:  global
        .offset:         8
        .size:           8
        .value_kind:     global_buffer
      - .address_space:  global
        .offset:         16
        .size:           8
        .value_kind:     global_buffer
      - .actual_access:  read_only
        .address_space:  global
        .offset:         24
        .size:           8
        .value_kind:     global_buffer
      - .actual_access:  read_only
        .address_space:  global
        .offset:         32
        .size:           8
        .value_kind:     global_buffer
      - .actual_access:  read_only
        .address_space:  global
        .offset:         40
        .size:           8
        .value_kind:     global_buffer
      - .offset:         48
        .size:           4
        .value_kind:     hidden_block_count_x
      - .offset:         52
        .size:           4
        .value_kind:     hidden_block_count_y
      - .offset:         56
        .size:           4
        .value_kind:     hidden_block_count_z
      - .offset:         60
        .size:           2
        .value_kind:     hidden_group_size_x
      - .offset:         62
        .size:           2
        .value_kind:     hidden_group_size_y
      - .offset:         64
        .size:           2
        .value_kind:     hidden_group_size_z
      - .offset:         66
        .size:           2
        .value_kind:     hidden_remainder_x
      - .offset:         68
        .size:           2
        .value_kind:     hidden_remainder_y
      - .offset:         70
        .size:           2
        .value_kind:     hidden_remainder_z
      - .offset:         88
        .size:           8
        .value_kind:     hidden_global_offset_x
      - .offset:         96
        .size:           8
        .value_kind:     hidden_global_offset_y
      - .offset:         104
        .size:           8
        .value_kind:     hidden_global_offset_z
      - .offset:         112
        .size:           2
        .value_kind:     hidden_grid_dims
    .group_segment_fixed_size: 1024
    .kernarg_segment_align: 8
    .kernarg_segment_size: 304
    .language:       OpenCL C
    .language_version:
      - 2
      - 0
    .max_flat_workgroup_size: 256
    .name:           _Z9bn_kernelPKDv8_DF16_S1_PS_PKfS4_S4_
    .private_segment_fixed_size: 0
    .sgpr_count:     20
    .sgpr_spill_count: 0
    .symbol:         _Z9bn_kernelPKDv8_DF16_S1_PS_PKfS4_S4_.kd
    .uniform_work_group_size: 1
    .uses_dynamic_stack: false
    .vgpr_count:     64
    .vgpr_spill_count: 0
    .wavefront_size: 64
  - .agpr_count:     0
    .args:
      - .actual_access:  read_only
        .address_space:  global
        .offset:         0
        .size:           8
        .value_kind:     global_buffer
      - .actual_access:  read_only
        .address_space:  global
        .offset:         8
        .size:           8
        .value_kind:     global_buffer
      - .actual_access:  read_only
        .address_space:  global
        .offset:         16
        .size:           8
        .value_kind:     global_buffer
      - .actual_access:  read_only
        .address_space:  global
        .offset:         24
        .size:           8
        .value_kind:     global_buffer
      - .actual_access:  read_only
        .address_space:  global
        .offset:         32
        .size:           8
        .value_kind:     global_buffer
      - .actual_access:  read_only
        .address_space:  global
        .offset:         40
        .size:           8
        .value_kind:     global_buffer
      - .actual_access:  read_only
        .address_space:  global
        .offset:         48
        .size:           8
        .value_kind:     global_buffer
      - .actual_access:  write_only
        .address_space:  global
        .offset:         56
        .size:           8
        .value_kind:     global_buffer
      - .offset:         64
        .size:           4
        .value_kind:     hidden_block_count_x
      - .offset:         68
        .size:           4
        .value_kind:     hidden_block_count_y
      - .offset:         72
        .size:           4
        .value_kind:     hidden_block_count_z
      - .offset:         76
        .size:           2
        .value_kind:     hidden_group_size_x
      - .offset:         78
        .size:           2
        .value_kind:     hidden_group_size_y
      - .offset:         80
        .size:           2
        .value_kind:     hidden_group_size_z
      - .offset:         82
        .size:           2
        .value_kind:     hidden_remainder_x
      - .offset:         84
        .size:           2
        .value_kind:     hidden_remainder_y
      - .offset:         86
        .size:           2
        .value_kind:     hidden_remainder_z
      - .offset:         104
        .size:           8
        .value_kind:     hidden_global_offset_x
      - .offset:         112
        .size:           8
        .value_kind:     hidden_global_offset_y
      - .offset:         120
        .size:           8
        .value_kind:     hidden_global_offset_z
      - .offset:         128
        .size:           2
        .value_kind:     hidden_grid_dims
    .group_segment_fixed_size: 34816
    .kernarg_segment_align: 8
    .kernarg_segment_size: 320
    .language:       OpenCL C
    .language_version:
      - 2
      - 0
    .max_flat_workgroup_size: 512
    .name:           _Z12final_kernelPKDv8_DF16_S1_PKfS3_S3_S1_S3_Pf
    .private_segment_fixed_size: 0
    .sgpr_count:     34
    .sgpr_spill_count: 0
    .symbol:         _Z12final_kernelPKDv8_DF16_S1_PKfS3_S3_S1_S3_Pf.kd
    .uniform_work_group_size: 1
    .uses_dynamic_stack: false
    .vgpr_count:     60
    .vgpr_spill_count: 0
    .wavefront_size: 64
  - .agpr_count:     0
    .args:
      - .actual_access:  read_only
        .address_space:  global
        .offset:         0
        .size:           8
        .value_kind:     global_buffer
      - .actual_access:  read_only
        .address_space:  global
        .offset:         8
        .size:           8
        .value_kind:     global_buffer
      - .address_space:  global
        .offset:         16
        .size:           8
        .value_kind:     global_buffer
      - .actual_access:  write_only
        .address_space:  global
        .offset:         24
        .size:           8
        .value_kind:     global_buffer
      - .address_space:  global
        .offset:         32
        .size:           8
        .value_kind:     global_buffer
      - .address_space:  global
        .offset:         40
        .size:           8
        .value_kind:     global_buffer
      - .actual_access:  read_only
        .address_space:  global
        .offset:         48
        .size:           8
        .value_kind:     global_buffer
      - .actual_access:  read_only
        .address_space:  global
        .offset:         56
        .size:           8
        .value_kind:     global_buffer
      - .address_space:  global
        .offset:         64
        .size:           8
        .value_kind:     global_buffer
      - .address_space:  global
        .offset:         72
        .size:           8
        .value_kind:     global_buffer
      - .actual_access:  read_only
        .address_space:  global
        .offset:         80
        .size:           8
        .value_kind:     global_buffer
      - .actual_access:  read_only
        .address_space:  global
        .offset:         88
        .size:           8
        .value_kind:     global_buffer
      - .offset:         96
        .size:           4
        .value_kind:     hidden_block_count_x
      - .offset:         100
        .size:           4
        .value_kind:     hidden_block_count_y
      - .offset:         104
        .size:           4
        .value_kind:     hidden_block_count_z
      - .offset:         108
        .size:           2
        .value_kind:     hidden_group_size_x
      - .offset:         110
        .size:           2
        .value_kind:     hidden_group_size_y
      - .offset:         112
        .size:           2
        .value_kind:     hidden_group_size_z
      - .offset:         114
        .size:           2
        .value_kind:     hidden_remainder_x
      - .offset:         116
        .size:           2
        .value_kind:     hidden_remainder_y
      - .offset:         118
        .size:           2
        .value_kind:     hidden_remainder_z
      - .offset:         136
        .size:           8
        .value_kind:     hidden_global_offset_x
      - .offset:         144
        .size:           8
        .value_kind:     hidden_global_offset_y
      - .offset:         152
        .size:           8
        .value_kind:     hidden_global_offset_z
      - .offset:         160
        .size:           2
        .value_kind:     hidden_grid_dims
    .group_segment_fixed_size: 26384
    .kernarg_segment_align: 8
    .kernarg_segment_size: 352
    .language:       OpenCL C
    .language_version:
      - 2
      - 0
    .max_flat_workgroup_size: 512
    .name:           _Z12layer_kernelILb1ELi512ELi64EEvPKDv8_DF16_PKfPS0_PiS6_S6_S2_S4_S5_PfPK15HIP_vector_typeIiLj2EEPKi
    .private_segment_fixed_size: 0
    .sgpr_count:     52
    .sgpr_spill_count: 0
    .symbol:         _Z12layer_kernelILb1ELi512ELi64EEvPKDv8_DF16_PKfPS0_PiS6_S6_S2_S4_S5_PfPK15HIP_vector_typeIiLj2EEPKi.kd
    .uniform_work_group_size: 1
    .uses_dynamic_stack: false
    .vgpr_count:     61
    .vgpr_spill_count: 0
    .wavefront_size: 64
  - .agpr_count:     0
    .args:
      - .actual_access:  read_only
        .address_space:  global
        .offset:         0
        .size:           8
        .value_kind:     global_buffer
      - .actual_access:  read_only
        .address_space:  global
        .offset:         8
        .size:           8
        .value_kind:     global_buffer
      - .actual_access:  read_only
        .address_space:  global
        .offset:         16
        .size:           8
        .value_kind:     global_buffer
      - .actual_access:  read_only
        .address_space:  global
        .offset:         24
        .size:           8
        .value_kind:     global_buffer
      - .actual_access:  read_only
        .address_space:  global
        .offset:         32
        .size:           8
        .value_kind:     global_buffer
      - .actual_access:  read_only
        .address_space:  global
        .offset:         40
        .size:           8
        .value_kind:     global_buffer
      - .actual_access:  read_only
        .address_space:  global
        .offset:         48
        .size:           8
        .value_kind:     global_buffer
      - .actual_access:  read_only
        .address_space:  global
        .offset:         56
        .size:           8
        .value_kind:     global_buffer
      - .address_space:  global
        .offset:         64
        .size:           8
        .value_kind:     global_buffer
      - .address_space:  global
        .offset:         72
        .size:           8
        .value_kind:     global_buffer
      - .actual_access:  read_only
        .address_space:  global
        .offset:         80
        .size:           8
        .value_kind:     global_buffer
      - .actual_access:  read_only
        .address_space:  global
        .offset:         88
        .size:           8
        .value_kind:     global_buffer
      - .offset:         96
        .size:           4
        .value_kind:     hidden_block_count_x
      - .offset:         100
        .size:           4
        .value_kind:     hidden_block_count_y
      - .offset:         104
        .size:           4
        .value_kind:     hidden_block_count_z
      - .offset:         108
        .size:           2
        .value_kind:     hidden_group_size_x
      - .offset:         110
        .size:           2
        .value_kind:     hidden_group_size_y
      - .offset:         112
        .size:           2
        .value_kind:     hidden_group_size_z
      - .offset:         114
        .size:           2
        .value_kind:     hidden_remainder_x
      - .offset:         116
        .size:           2
        .value_kind:     hidden_remainder_y
      - .offset:         118
        .size:           2
        .value_kind:     hidden_remainder_z
      - .offset:         136
        .size:           8
        .value_kind:     hidden_global_offset_x
      - .offset:         144
        .size:           8
        .value_kind:     hidden_global_offset_y
      - .offset:         152
        .size:           8
        .value_kind:     hidden_global_offset_z
      - .offset:         160
        .size:           2
        .value_kind:     hidden_grid_dims
    .group_segment_fixed_size: 22000
    .kernarg_segment_align: 8
    .kernarg_segment_size: 352
    .language:       OpenCL C
    .language_version:
      - 2
      - 0
    .max_flat_workgroup_size: 256
    .name:           _Z12layer_kernelILb0ELi256ELi32EEvPKDv8_DF16_PKfPS0_PiS6_S6_S2_S4_S5_PfPK15HIP_vector_typeIiLj2EEPKi
    .private_segment_fixed_size: 0
    .sgpr_count:     36
    .sgpr_spill_count: 0
    .symbol:         _Z12layer_kernelILb0ELi256ELi32EEvPKDv8_DF16_PKfPS0_PiS6_S6_S2_S4_S5_PfPK15HIP_vector_typeIiLj2EEPKi.kd
    .uniform_work_group_size: 1
    .uses_dynamic_stack: false
    .vgpr_count:     64
    .vgpr_spill_count: 0
    .wavefront_size: 64
